# strategy 5 direct HBM->LDS: gla_p_unit's per-head WUP/BAL staging by LDS-DMA (one 1 KB piece per wave, one wait) instead of load/wait/ds_write loops; on top of m21
# baseline (speedup 1.0000x reference)
; #define GAS __attribute__((address_space(1)))
; DI void gla_p_unit(LAS unsigned char* lds, const Ctx& c, int l, int bl, int h, int n, int& h_loaded) {
;     ...
;     if (h_loaded != h) { for (int i = tid; i < 16 * 128; i += NTHREADS) WUP[i] = ((const GAS float*)c.w_alpha_up)[(size_t)l * 16 * 512 + (i >> 7) * 512 + h * 128 + (i & 127)];
;         if (tid < 128) BAL[tid] = ((const GAS float*)c.b_alpha)[l * 512 + h * 128 + tid]; h_loaded = h; __syncthreads(); }
.LBB0_564:
	s_bfe_u32 s6, s38, 0x20006
	s_waitcnt vmcnt(0)
	v_mov_b32_e32 v2, v0
	s_lshl_b32 s7, s6, 7
	s_cmp_eq_u32 s63, s6
	v_readfirstlane_b32 s67, v2
	s_barrier
	s_cbranch_scc1 .LBB0_576
	s_mov_b32 s8, m0
	v_lshrrev_b32_e32 v1, 5, v2
	v_and_b32_e32 v3, 31, v2
	v_lshlrev_b32_e32 v1, 11, v1
	v_lshl_add_u32 v6, v3, 4, v1
	v_mov_b32_e32 v7, v4
	s_lshl_b32 s30, s7, 2
	v_add_u32_e32 v6, s30, v6
	v_lshl_add_u64 v[6:7], s[16:17], 0, v[6:7]
	s_lshl_b32 s30, s67, 4
	s_add_i32 s30, s48, s30
	s_mov_b32 m0, s30
	s_nop 0
	global_load_lds_dwordx4 v[6:7], off
	s_cmpk_gt_u32 s67, 0x7f
	s_cbranch_scc1 .Lp_nobal
	v_readlane_b32 s30, v254, 36
	s_add_i32 s30, s7, s30
	s_nop 1
	v_add_u32_e32 v6, s30, v2
	v_ashrrev_i32_e32 v7, 31, v6
	v_lshl_add_u64 v[6:7], v[6:7], 2, s[42:43]
	s_lshl_b32 s30, s67, 2
	s_add_i32 s30, s49, s30
	s_mov_b32 m0, s30
	s_nop 0
	global_load_lds_dword v[6:7], off
.Lp_nobal:
	s_mov_b32 m0, s8
	s_mov_b32 s63, s6
	s_waitcnt vmcnt(0)
	s_barrier
